# outtouch1
# baseline (speedup 1.0000x reference)
_Z11attn_kernelILi4EEvPKfS1_S1_S1_S1_S1_PKcPf:
	s_load_dwordx2 s[24:25], s[0:1], 0x30
	s_load_dwordx8 s[8:15], s[0:1], 0x0
	s_load_dwordx4 s[16:19], s[0:1], 0x20
	s_load_dwordx2 s[34:35], s[0:1], 0x38
	v_lshrrev_b32_e32 v63, 6, v0
	v_and_b32_e32 v57, 15, v0
	v_bfe_u32 v1, v0, 4, 2
	v_lshrrev_b32_e32 v2, 2, v57
	v_mul_u32_u24_e32 v4, 3, v1
	v_mul_u32_u24_e32 v2, 3, v2
	v_mad_u32_u24 v4, v63, 12, v4
	v_mad_u32_u24 v2, v63, 12, v2
	v_lshlrev_b32_e32 v4, 2, v4
	v_lshlrev_b32_e32 v2, 2, v2
	v_and_b32_e32 v104, 63, v0
	v_lshlrev_b32_e32 v60, 5, v57
	v_lshlrev_b32_e32 v58, 3, v1
	v_add_u32_e32 v3, v60, v58
	v_lshrrev_b32_e32 v56, 4, v0
	v_lshlrev_b32_e32 v54, 4, v57
	v_mov_b32_e32 v59, 0
	s_movk_i32 s4, 0xe0
	v_cmp_gt_u32_e64 s[4:5], s4, v0
	s_lshl_b32 s26, s2, 8
	s_lshl_b32 s27, s2, 9
	s_mul_i32 s28, s2, 14
	s_add_u32 s26, s26, 0x164000
	s_add_u32 s27, s27, 0x80000
	s_add_u32 s20, s26, 0xc0
	v_lshlrev_b32_e32 v5, 2, v57
	v_lshlrev_b32_e32 v147, 6, v57
	v_add_u32_e32 v2, s26, v2
	v_add_u32_e32 v4, s26, v4
	v_add_u32_e32 v3, s27, v3
	v_mul_u32_u24_e32 v156, 0x140, v1
	s_movk_i32 s21, 0x500
	v_mad_u32_u24 v156, v63, s21, v156
	v_lshl_or_b32 v156, v57, 2, v156
	v_add_u32_e32 v156, 0x1c00, v156
	v_lshlrev_b32_e32 v157, 5, v56
	v_cmp_gt_u32_e32 vcc, 3, v57
	v_add_u32_e32 v158, 4, v57
	v_lshlrev_b32_e32 v159, 2, v57
	s_movk_i32 s21, 0x50
	v_cndmask_b32_e32 v158, 4, v158, vcc
	v_mad_u32_u24 v159, v56, s21, v159
	v_lshl_add_u32 v158, v158, 2, v157
	v_mul_u32_u24_e32 v250, 0x50, v56
	v_or_b32_e32 v250, 0x3800, v250
	v_lshl_add_u32 v251, v57, 1, v250
	v_mul_u32_u24_e32 v252, 0x50, v57
	v_lshl_add_u32 v252, v58, 1, v252
	v_lshlrev_b32_e32 v253, 2, v57
	v_and_b32_e32 v254, 0xc0, v0
	v_lshlrev_b32_e32 v255, 11, v1
	v_or3_b32 v253, v253, v254, v255
	v_add_u32_e32 v254, s28, v56
	v_lshl_add_u32 v254, v254, 9, v54
	v_lshl_or_b32 v255, v56, 9, v54
	s_waitcnt lgkmcnt(0)
	global_load_dwordx3 v[80:82], v2, s[24:25]
	global_load_dwordx3 v[84:86], v4, s[24:25]
	global_load_dwordx2 v[64:65], v3, s[24:25]
	s_load_dword s3, s[24:25], s20
	s_add_u32 s22, s24, 0x160000
	s_addc_u32 s23, s25, 0
	v_cndmask_b32_e64 v62, 13, v56, s[4:5]
	v_add_u32_e32 v3, s28, v62
	v_mad_u32_u24 v144, v3, 36, v5
	v_mad_u32_u24 v146, v3, 12, v5
	v_add_u32_e32 v145, -36, v146
	v_add_u32_e32 v146, -48, v146
	v_lshl_or_b32 v147, v63, 10, v147
	v_lshl_or_b32 v147, v1, 4, v147
	v_or_b32_e32 v148, 0x1000, v147
	v_lshlrev_b32_e32 v149, 4, v104
	v_lshlrev_b32_e32 v150, 9, v3
	v_add_u32_e32 v150, v150, v54
	v_and_b32_e32 v87, 3, v57
	v_lshlrev_b32_e32 v87, 4, v87
	v_lshl_or_b32 v87, v1, 6, v87
	v_lshlrev_b32_e32 v88, 3, v57
	s_add_u32 s26, s24, 0x100000
	s_addc_u32 s27, s25, 0
	s_add_u32 s28, s24, 0x140000
	s_addc_u32 s29, s25, 0
	s_movk_i32 s6, 0x140
	v_cmp_gt_u32_e32 vcc, s6, v0
	v_lshlrev_b32_e32 v22, 2, v0
	v_mov_b32_e32 v23, 0
	s_and_saveexec_b64 s[6:7], vcc
	ds_write_b32 v22, v23 offset:14336
	s_or_b64 exec, exec, s[6:7]
	v_cmp_gt_u32_e32 vcc, 64, v0
	s_and_saveexec_b64 s[6:7], vcc
	ds_write_b32 v22, v23 offset:15360
	s_or_b64 exec, exec, s[6:7]
	v_mov_b32_e32 v45, 0xc9c35000
	s_mov_b32 s30, 0x3db8aa3b
	s_mov_b32 s31, 0x3db8aa3b
	v_mov_b32_e32 v121, 0x3fb8aa3b
	v_mov_b32_e32 v35, 0
	v_mov_b32_e32 v44, v45
	s_waitcnt lgkmcnt(0)
	s_bitcmp0_b32 s3, 1
	s_cselect_b64 s[20:21], -1, 0
	s_cbranch_scc1 .LBB1_16
	v_bfe_u32 v46, s3, v57, 1
	v_cmp_eq_u32_e32 vcc, 0, v46
	s_nop 1
	v_cndmask_b32_e32 v47, 0, v45, vcc
	v_cndmask_b32_e64 v55, 1.0, 0, vcc
	s_nop 0
	v_mov_b32_dpp v34, v47 row_newbcast:0 row_mask:0xf bank_mask:0xf bound_ctrl:1
	v_mov_b32_dpp v36, v47 row_newbcast:2 row_mask:0xf bank_mask:0xf bound_ctrl:1
	v_mov_b32_dpp v37, v47 row_newbcast:3 row_mask:0xf bank_mask:0xf bound_ctrl:1
	v_mov_b32_dpp v22, v47 row_newbcast:4 row_mask:0xf bank_mask:0xf bound_ctrl:1
	v_mov_b32_dpp v23, v47 row_newbcast:5 row_mask:0xf bank_mask:0xf bound_ctrl:1
	v_mov_b32_dpp v24, v47 row_newbcast:6 row_mask:0xf bank_mask:0xf bound_ctrl:1
	v_mov_b32_dpp v25, v47 row_newbcast:7 row_mask:0xf bank_mask:0xf bound_ctrl:1
	v_mov_b32_dpp v38, v47 row_newbcast:8 row_mask:0xf bank_mask:0xf bound_ctrl:1
	v_mov_b32_dpp v39, v47 row_newbcast:9 row_mask:0xf bank_mask:0xf bound_ctrl:1
	v_mov_b32_dpp v40, v47 row_newbcast:10 row_mask:0xf bank_mask:0xf bound_ctrl:1
	v_mov_b32_dpp v41, v47 row_newbcast:11 row_mask:0xf bank_mask:0xf bound_ctrl:1
	v_mov_b32_dpp v42, v47 row_newbcast:12 row_mask:0xf bank_mask:0xf bound_ctrl:1
	v_mov_b32_dpp v43, v47 row_newbcast:13 row_mask:0xf bank_mask:0xf bound_ctrl:1
	s_waitcnt vmcnt(1)
	v_lshl_add_u32 v72, v80, 9, v87
	v_lshl_add_u32 v73, v81, 9, v87
	v_lshl_add_u32 v74, v82, 9, v87
	global_load_dwordx4 v[50:53], v72, s[24:25]
	global_load_dwordx4 v[46:49], v72, s[24:25] offset:256
	global_load_dwordx4 v[14:17], v73, s[24:25]
	global_load_dwordx4 v[10:13], v73, s[24:25] offset:256
	global_load_dwordx4 v[6:9], v74, s[24:25]
	global_load_dwordx4 v[2:5], v74, s[24:25] offset:256
	v_lshl_add_u32 v75, v84, 8, v54
	v_lshl_add_u32 v78, v84, 7, v88
	v_lshl_add_u32 v76, v85, 8, v54
	v_lshl_add_u32 v79, v85, 7, v88
	v_lshl_add_u32 v77, v86, 8, v54
	v_lshl_add_u32 v80, v86, 7, v88
	global_load_dwordx4 v[30:33], v75, s[26:27]
	global_load_dwordx2 v[70:71], v78, s[28:29]
	global_load_dwordx4 v[26:29], v76, s[26:27]
	global_load_dwordx2 v[66:67], v79, s[28:29]
	global_load_dwordx4 v[18:21], v77, s[26:27]
	global_load_dwordx2 v[68:69], v80, s[28:29]
	s_mov_b32 exec_lo, 0x1ff01ff
	s_mov_b32 exec_hi, 0x1ff01ff
	global_load_dword v120, v144, s[10:11]
	s_mov_b32 exec_lo, 0xe000e00
	s_mov_b32 exec_hi, 0xe000e00
	global_load_dword v120, v145, s[12:13]
	s_mov_b32 exec_lo, 0x70007000
	s_mov_b32 exec_hi, 0x70007000
	global_load_dword v120, v146, s[14:15]
	s_mov_b64 exec, -1
	global_load_dwordx4 v[124:127], v147, s[22:23]
	global_load_dwordx4 v[128:131], v148, s[22:23]
	s_mov_b32 exec_hi, 0
	global_load_dwordx4 v[132:135], v149, s[16:17]
	s_mov_b32 exec_hi, -1
	s_mov_b32 exec_lo, 0
	global_load_dwordx4 v[132:135], v149, s[18:19] offset:-512
	s_mov_b32 exec_lo, -1
	global_load_dwordx4 v[136:139], v150, s[8:9]
	global_load_dwordx4 v[140:143], v150, s[8:9] offset:256
	s_mov_b64 exec, 1
	global_load_dword v119, v150, s[34:35]
	s_mov_b64 exec, -1
	v_mov_b32_e32 v75, 0
	v_mov_b32_e32 v79, 0
	v_mov_b32_e32 v83, 0
	s_waitcnt vmcnt(21)
	v_mfma_f32_16x16x32_fp8_fp8 v[160:163], v[50:51], v[64:65], v[34:37]
	v_mfma_f32_16x16x32_fp8_fp8 v[164:167], v[52:53], v[64:65], v[22:25]
	s_waitcnt vmcnt(20)
	v_mfma_f32_16x16x32_fp8_fp8 v[168:171], v[46:47], v[64:65], v[38:41]
	v_mfma_f32_16x16x32_fp8_fp8 v[172:175], v[48:49], v[64:65], v[42:45]
	s_nop 3
	v_max3_f32 v86, v160, v161, v162
	v_max3_f32 v87, v163, v164, v165
	v_max3_f32 v88, v166, v167, v168
	v_max3_f32 v89, v169, v170, v171
	v_max3_f32 v86, v86, v172, v173
	v_max3_f32 v87, v87, v88, v89
	v_max_f32_e32 v96, v86, v87
	v_mul_f32_e32 v98, 0xbdb8aa3b, v96
	v_pk_fma_f32 v[208:209], v[160:161], s[30:31], v[98:99] op_sel_hi:[1,1,0]
	v_pk_fma_f32 v[210:211], v[162:163], s[30:31], v[98:99] op_sel_hi:[1,1,0]
	v_pk_fma_f32 v[212:213], v[164:165], s[30:31], v[98:99] op_sel_hi:[1,1,0]
	v_pk_fma_f32 v[214:215], v[166:167], s[30:31], v[98:99] op_sel_hi:[1,1,0]
	v_pk_fma_f32 v[216:217], v[168:169], s[30:31], v[98:99] op_sel_hi:[1,1,0]
	v_pk_fma_f32 v[218:219], v[170:171], s[30:31], v[98:99] op_sel_hi:[1,1,0]
	v_pk_fma_f32 v[220:221], v[172:173], s[30:31], v[98:99] op_sel_hi:[1,1,0]
	v_exp_f32_e32 v208, v208
	v_exp_f32_e32 v209, v209
	v_exp_f32_e32 v210, v210
	v_exp_f32_e32 v211, v211
	v_exp_f32_e32 v212, v212
	v_exp_f32_e32 v213, v213
	v_exp_f32_e32 v214, v214
	v_exp_f32_e32 v215, v215
	v_exp_f32_e32 v216, v216
	v_exp_f32_e32 v217, v217
	v_exp_f32_e32 v218, v218
	v_exp_f32_e32 v219, v219
	v_exp_f32_e32 v220, v220
	v_exp_f32_e32 v221, v221
	s_waitcnt vmcnt(19)
	v_mfma_f32_16x16x32_fp8_fp8 v[176:179], v[14:15], v[64:65], v[34:37]
	v_mfma_f32_16x16x32_fp8_fp8 v[180:183], v[16:17], v[64:65], v[22:25]
	s_waitcnt vmcnt(18)
	v_mfma_f32_16x16x32_fp8_fp8 v[184:187], v[10:11], v[64:65], v[38:41]
	v_mfma_f32_16x16x32_fp8_fp8 v[188:191], v[12:13], v[64:65], v[42:45]
	v_pk_add_f32 v[86:87], v[208:209], v[210:211]
	v_pk_add_f32 v[88:89], v[212:213], v[214:215]
	v_pk_add_f32 v[90:91], v[216:217], v[218:219]
	v_pk_mul_f32 v[92:93], v[208:209], v[160:161]
	v_pk_mul_f32 v[94:95], v[210:211], v[162:163]
	v_pk_add_f32 v[86:87], v[86:87], v[220:221]
	v_pk_add_f32 v[88:89], v[88:89], v[90:91]
	v_pk_fma_f32 v[92:93], v[212:213], v[164:165], v[92:93]
	v_pk_fma_f32 v[94:95], v[214:215], v[166:167], v[94:95]
	v_pk_add_f32 v[86:87], v[86:87], v[88:89]
	v_pk_fma_f32 v[92:93], v[216:217], v[168:169], v[92:93]
	v_pk_fma_f32 v[94:95], v[218:219], v[170:171], v[94:95]
	v_add_f32_e32 v86, v86, v87
	v_pk_fma_f32 v[92:93], v[220:221], v[172:173], v[92:93]
	v_rcp_f32_e32 v87, v86
	v_pk_add_f32 v[92:93], v[92:93], v[94:95]
	v_mul_f32_e32 v87, v55, v87
	v_add_f32_e32 v92, v92, v93
	v_mul_f32_e32 v107, v86, v87
	v_mul_f32_e32 v92, v92, v87
	v_mul_f32_e32 v100, 0x43800000, v87
	v_mul_f32_e32 v103, 0x3d800000, v92
	v_max3_f32 v86, v176, v177, v178
	v_max3_f32 v87, v179, v180, v181
	v_max3_f32 v88, v182, v183, v184
	v_max3_f32 v89, v185, v186, v187
	v_max3_f32 v86, v86, v188, v189
	v_max3_f32 v87, v87, v88, v89
	v_max_f32_e32 v96, v86, v87
	v_mul_f32_e32 v98, 0xbdb8aa3b, v96
	v_pk_fma_f32 v[222:223], v[176:177], s[30:31], v[98:99] op_sel_hi:[1,1,0]
	v_pk_fma_f32 v[224:225], v[178:179], s[30:31], v[98:99] op_sel_hi:[1,1,0]
	v_pk_fma_f32 v[226:227], v[180:181], s[30:31], v[98:99] op_sel_hi:[1,1,0]
	v_pk_fma_f32 v[228:229], v[182:183], s[30:31], v[98:99] op_sel_hi:[1,1,0]
	v_pk_fma_f32 v[230:231], v[184:185], s[30:31], v[98:99] op_sel_hi:[1,1,0]
	v_pk_fma_f32 v[232:233], v[186:187], s[30:31], v[98:99] op_sel_hi:[1,1,0]
	v_pk_fma_f32 v[234:235], v[188:189], s[30:31], v[98:99] op_sel_hi:[1,1,0]
	v_exp_f32_e32 v222, v222
	v_exp_f32_e32 v223, v223
	v_exp_f32_e32 v224, v224
	v_exp_f32_e32 v225, v225
	v_exp_f32_e32 v226, v226
	v_exp_f32_e32 v227, v227
	v_exp_f32_e32 v228, v228
	v_exp_f32_e32 v229, v229
	v_exp_f32_e32 v230, v230
	v_exp_f32_e32 v231, v231
	v_exp_f32_e32 v232, v232
	v_exp_f32_e32 v233, v233
	v_exp_f32_e32 v234, v234
	v_exp_f32_e32 v235, v235
	s_waitcnt vmcnt(17)
	v_mfma_f32_16x16x32_fp8_fp8 v[192:195], v[6:7], v[64:65], v[34:37]
	v_mfma_f32_16x16x32_fp8_fp8 v[196:199], v[8:9], v[64:65], v[22:25]
	s_waitcnt vmcnt(16)
	v_mfma_f32_16x16x32_fp8_fp8 v[200:203], v[2:3], v[64:65], v[38:41]
	v_mfma_f32_16x16x32_fp8_fp8 v[204:207], v[4:5], v[64:65], v[42:45]
	v_pk_add_f32 v[86:87], v[222:223], v[224:225]
	v_pk_add_f32 v[88:89], v[226:227], v[228:229]
	v_pk_add_f32 v[90:91], v[230:231], v[232:233]
	v_pk_mul_f32 v[92:93], v[222:223], v[176:177]
	v_pk_mul_f32 v[94:95], v[224:225], v[178:179]
	v_pk_add_f32 v[86:87], v[86:87], v[234:235]
	v_pk_add_f32 v[88:89], v[88:89], v[90:91]
	v_pk_fma_f32 v[92:93], v[226:227], v[180:181], v[92:93]
	v_pk_fma_f32 v[94:95], v[228:229], v[182:183], v[94:95]
	v_pk_add_f32 v[86:87], v[86:87], v[88:89]
	v_pk_fma_f32 v[92:93], v[230:231], v[184:185], v[92:93]
	v_pk_fma_f32 v[94:95], v[232:233], v[186:187], v[94:95]
	v_add_f32_e32 v86, v86, v87
	v_pk_fma_f32 v[92:93], v[234:235], v[188:189], v[92:93]
	v_rcp_f32_e32 v87, v86
	v_pk_add_f32 v[92:93], v[92:93], v[94:95]
	v_mul_f32_e32 v87, v55, v87
	v_add_f32_e32 v92, v92, v93
	v_mul_f32_e32 v108, v86, v87
	v_mul_f32_e32 v92, v92, v87
	v_mul_f32_e32 v101, 0x43800000, v87
	v_mul_f32_e32 v105, 0x3d800000, v92
	v_max3_f32 v86, v192, v193, v194
	v_max3_f32 v87, v195, v196, v197
	v_max3_f32 v88, v198, v199, v200
	v_max3_f32 v89, v201, v202, v203
	v_max3_f32 v86, v86, v204, v205
	v_max3_f32 v87, v87, v88, v89
	v_max_f32_e32 v96, v86, v87
	v_mul_f32_e32 v98, 0xbdb8aa3b, v96
	v_pk_fma_f32 v[236:237], v[192:193], s[30:31], v[98:99] op_sel_hi:[1,1,0]
	v_pk_fma_f32 v[238:239], v[194:195], s[30:31], v[98:99] op_sel_hi:[1,1,0]
	v_pk_fma_f32 v[240:241], v[196:197], s[30:31], v[98:99] op_sel_hi:[1,1,0]
	v_pk_fma_f32 v[242:243], v[198:199], s[30:31], v[98:99] op_sel_hi:[1,1,0]
	v_pk_fma_f32 v[244:245], v[200:201], s[30:31], v[98:99] op_sel_hi:[1,1,0]
	v_pk_fma_f32 v[246:247], v[202:203], s[30:31], v[98:99] op_sel_hi:[1,1,0]
	v_pk_fma_f32 v[248:249], v[204:205], s[30:31], v[98:99] op_sel_hi:[1,1,0]
	v_exp_f32_e32 v236, v236
	v_exp_f32_e32 v237, v237
	v_exp_f32_e32 v238, v238
	v_exp_f32_e32 v239, v239
	v_exp_f32_e32 v240, v240
	v_exp_f32_e32 v241, v241
	v_exp_f32_e32 v242, v242
	v_exp_f32_e32 v243, v243
	v_exp_f32_e32 v244, v244
	v_exp_f32_e32 v245, v245
	v_exp_f32_e32 v246, v246
	v_exp_f32_e32 v247, v247
	v_exp_f32_e32 v248, v248
	v_exp_f32_e32 v249, v249
	v_pk_add_f32 v[86:87], v[236:237], v[238:239]
	v_pk_add_f32 v[88:89], v[240:241], v[242:243]
	v_pk_add_f32 v[90:91], v[244:245], v[246:247]
	v_pk_mul_f32 v[92:93], v[236:237], v[192:193]
	v_pk_mul_f32 v[94:95], v[238:239], v[194:195]
	v_pk_add_f32 v[86:87], v[86:87], v[248:249]
	v_pk_add_f32 v[88:89], v[88:89], v[90:91]
	v_pk_fma_f32 v[92:93], v[240:241], v[196:197], v[92:93]
	v_pk_fma_f32 v[94:95], v[242:243], v[198:199], v[94:95]
	v_pk_add_f32 v[86:87], v[86:87], v[88:89]
	v_pk_fma_f32 v[92:93], v[244:245], v[200:201], v[92:93]
	v_pk_fma_f32 v[94:95], v[246:247], v[202:203], v[94:95]
	v_add_f32_e32 v86, v86, v87
	v_pk_fma_f32 v[92:93], v[248:249], v[204:205], v[92:93]
	v_rcp_f32_e32 v87, v86
	v_pk_add_f32 v[92:93], v[92:93], v[94:95]
	v_mul_f32_e32 v87, v55, v87
	v_add_f32_e32 v92, v92, v93
	v_mul_f32_e32 v109, v86, v87
	v_mul_f32_e32 v92, v92, v87
	v_mul_f32_e32 v102, 0x43800000, v87
	v_mul_f32_e32 v106, 0x3d800000, v92
	v_max3_f32 v122, v103, v105, v106
	v_cmp_gt_u32_e64 s[6:7], 16, v104
	v_mov_b32_e32 v123, v122
	s_nop 1
	v_permlane16_swap_b32_e32 v122, v123
	v_max_f32_e32 v122, v122, v123
	v_mov_b32_e32 v123, v122
	s_nop 1
	v_permlane32_swap_b32_e32 v122, v123
	v_max_f32_e32 v36, v122, v123
	v_mul_f32_e32 v123, 0x3fb8aa3b, v36
	v_fma_f32 v111, v103, v121, -v123
	v_exp_f32_e32 v111, v111
	s_nop 0
	v_mul_f32_e32 v112, v111, v100
	v_mul_f32_e32 v110, v111, v107
	v_mov_b32_e32 v114, v111
	v_pk_mul_f32 v[208:209], v[208:209], v[112:113] op_sel_hi:[1,0]
	v_pk_mul_f32 v[210:211], v[210:211], v[112:113] op_sel_hi:[1,0]
	v_pk_mul_f32 v[212:213], v[212:213], v[112:113] op_sel_hi:[1,0]
	v_pk_mul_f32 v[214:215], v[214:215], v[112:113] op_sel_hi:[1,0]
	v_pk_mul_f32 v[216:217], v[216:217], v[112:113] op_sel_hi:[1,0]
	v_pk_mul_f32 v[218:219], v[218:219], v[112:113] op_sel_hi:[1,0]
	v_pk_mul_f32 v[220:221], v[220:221], v[112:113] op_sel_hi:[1,0]
	s_waitcnt vmcnt(14)
	v_mov_b32_e32 v115, v110
	v_fma_mix_f32 v116, v110, v70, 0 op_sel_hi:[0,1,0]
	v_fma_mix_f32 v117, v110, v70, 0 op_sel:[0,1,0] op_sel_hi:[0,1,0]
	v_fma_mix_f32 v118, v110, v71, 0 op_sel_hi:[0,1,0]
	v_cvt_pk_fp8_f32 v72, v208, v209
	v_cvt_pk_fp8_f32 v73, v212, v213
	v_cvt_pk_fp8_f32 v74, v216, v217
	v_cvt_pk_fp8_f32 v75, v220, v221
	v_cvt_pk_fp8_f32 v72, v210, v211 op_sel:[0,0,1]
	v_cvt_pk_fp8_f32 v73, v214, v215 op_sel:[0,0,1]
	v_cvt_pk_fp8_f32 v74, v218, v219 op_sel:[0,0,1]
	s_nop 1
	v_mfma_f32_16x16x32_fp8_fp8 v[152:155], v[72:73], v[30:31], 0
	v_mfma_f32_16x16x32_fp8_fp8 v[152:155], v[74:75], v[32:33], v[152:155]
	v_fma_f32 v111, v105, v121, -v123
	v_exp_f32_e32 v111, v111
	s_nop 0
	v_mul_f32_e32 v112, v111, v101
	v_mul_f32_e32 v110, v111, v108
	v_add_f32_e32 v114, v114, v111
	v_pk_mul_f32 v[222:223], v[222:223], v[112:113] op_sel_hi:[1,0]
	v_pk_mul_f32 v[224:225], v[224:225], v[112:113] op_sel_hi:[1,0]
	v_pk_mul_f32 v[226:227], v[226:227], v[112:113] op_sel_hi:[1,0]
	v_pk_mul_f32 v[228:229], v[228:229], v[112:113] op_sel_hi:[1,0]
	v_pk_mul_f32 v[230:231], v[230:231], v[112:113] op_sel_hi:[1,0]
	v_pk_mul_f32 v[232:233], v[232:233], v[112:113] op_sel_hi:[1,0]
	v_pk_mul_f32 v[234:235], v[234:235], v[112:113] op_sel_hi:[1,0]
	s_waitcnt vmcnt(12)
	v_add_f32_e32 v115, v115, v110
	v_fma_mix_f32 v116, v110, v66, v116 op_sel_hi:[0,1,0]
	v_fma_mix_f32 v117, v110, v66, v117 op_sel:[0,1,0] op_sel_hi:[0,1,0]
	v_fma_mix_f32 v118, v110, v67, v118 op_sel_hi:[0,1,0]
	v_cvt_pk_fp8_f32 v76, v222, v223
	v_cvt_pk_fp8_f32 v77, v226, v227
	v_cvt_pk_fp8_f32 v78, v230, v231
	v_cvt_pk_fp8_f32 v79, v234, v235
	v_cvt_pk_fp8_f32 v76, v224, v225 op_sel:[0,0,1]
	v_cvt_pk_fp8_f32 v77, v228, v229 op_sel:[0,0,1]
	v_cvt_pk_fp8_f32 v78, v232, v233 op_sel:[0,0,1]
	s_nop 1
	v_mfma_f32_16x16x32_fp8_fp8 v[152:155], v[76:77], v[26:27], v[152:155]
	v_mfma_f32_16x16x32_fp8_fp8 v[152:155], v[78:79], v[28:29], v[152:155]
	v_fma_f32 v111, v106, v121, -v123
	v_exp_f32_e32 v111, v111
	s_nop 0
	v_mul_f32_e32 v112, v111, v102
	v_mul_f32_e32 v110, v111, v109
	v_add_f32_e32 v114, v114, v111
	v_pk_mul_f32 v[236:237], v[236:237], v[112:113] op_sel_hi:[1,0]
	v_pk_mul_f32 v[238:239], v[238:239], v[112:113] op_sel_hi:[1,0]
	v_pk_mul_f32 v[240:241], v[240:241], v[112:113] op_sel_hi:[1,0]
	v_pk_mul_f32 v[242:243], v[242:243], v[112:113] op_sel_hi:[1,0]
	v_pk_mul_f32 v[244:245], v[244:245], v[112:113] op_sel_hi:[1,0]
	v_pk_mul_f32 v[246:247], v[246:247], v[112:113] op_sel_hi:[1,0]
	v_pk_mul_f32 v[248:249], v[248:249], v[112:113] op_sel_hi:[1,0]
	s_waitcnt vmcnt(10)
	v_add_f32_e32 v115, v115, v110
	v_fma_mix_f32 v116, v110, v68, v116 op_sel_hi:[0,1,0]
	v_fma_mix_f32 v117, v110, v68, v117 op_sel:[0,1,0] op_sel_hi:[0,1,0]
	v_fma_mix_f32 v118, v110, v69, v118 op_sel_hi:[0,1,0]
	v_cvt_pk_fp8_f32 v80, v236, v237
	v_cvt_pk_fp8_f32 v81, v240, v241
	v_cvt_pk_fp8_f32 v82, v244, v245
	v_cvt_pk_fp8_f32 v83, v248, v249
	v_cvt_pk_fp8_f32 v80, v238, v239 op_sel:[0,0,1]
	v_cvt_pk_fp8_f32 v81, v242, v243 op_sel:[0,0,1]
	v_cvt_pk_fp8_f32 v82, v246, v247 op_sel:[0,0,1]
	s_nop 1
	v_mfma_f32_16x16x32_fp8_fp8 v[152:155], v[80:81], v[18:19], v[152:155]
	v_mfma_f32_16x16x32_fp8_fp8 v[152:155], v[82:83], v[20:21], v[152:155]
	v_mov_b32_e32 v86, v114
	v_mov_b32_e32 v87, v115
	v_mov_b32_e32 v88, v116
	v_mov_b32_e32 v89, v117
	v_mov_b32_e32 v90, v118
	v_permlane16_swap_b32_e32 v114, v86
	v_permlane16_swap_b32_e32 v115, v87
	v_permlane16_swap_b32_e32 v116, v88
	v_permlane16_swap_b32_e32 v117, v89
	v_permlane16_swap_b32_e32 v118, v90
	v_add_f32_e32 v114, v114, v86
	v_add_f32_e32 v115, v115, v87
	v_add_f32_e32 v116, v116, v88
	v_add_f32_e32 v117, v117, v89
	v_add_f32_e32 v118, v118, v90
	v_mov_b32_e32 v86, v114
	v_mov_b32_e32 v87, v115
	v_mov_b32_e32 v88, v116
	v_mov_b32_e32 v89, v117
	v_mov_b32_e32 v90, v118
	v_permlane32_swap_b32_e32 v114, v86
	v_permlane32_swap_b32_e32 v115, v87
	v_permlane32_swap_b32_e32 v116, v88
	v_permlane32_swap_b32_e32 v117, v89
	v_permlane32_swap_b32_e32 v118, v90
	v_add_f32_e32 v37, v114, v86
	v_add_f32_e32 v20, v115, v87
	v_add_f32_e32 v18, v116, v88
	v_add_f32_e32 v19, v117, v89
	v_add_f32_e32 v21, v118, v90
	ds_write2_b32 v156, v152, v153 offset0:0 offset1:20
	ds_write2_b32 v156, v154, v155 offset0:40 offset1:60
	s_branch .LBB1_30
.LBB1_16:
	s_mov_b32 exec_lo, 0x1ff01ff
	s_mov_b32 exec_hi, 0x1ff01ff
	global_load_dword v120, v144, s[10:11]
	s_mov_b32 exec_lo, 0xe000e00
	s_mov_b32 exec_hi, 0xe000e00
	global_load_dword v120, v145, s[12:13]
	s_mov_b32 exec_lo, 0x70007000
	s_mov_b32 exec_hi, 0x70007000
	global_load_dword v120, v146, s[14:15]
	s_mov_b64 exec, -1
	global_load_dwordx4 v[124:127], v147, s[22:23]
	global_load_dwordx4 v[128:131], v148, s[22:23]
	s_mov_b32 exec_hi, 0
	global_load_dwordx4 v[132:135], v149, s[16:17]
	s_mov_b32 exec_hi, -1
	s_mov_b32 exec_lo, 0
	global_load_dwordx4 v[132:135], v149, s[18:19] offset:-512
	s_mov_b32 exec_lo, -1
	global_load_dwordx4 v[136:139], v150, s[8:9]
	global_load_dwordx4 v[140:143], v150, s[8:9] offset:256
	s_mov_b64 exec, 1
	global_load_dword v119, v150, s[34:35]
	s_mov_b64 exec, -1
	v_mov_b32_e32 v21, 0
	ds_write2_b32 v156, v21, v21 offset1:20
	ds_write2_b32 v156, v21, v21 offset0:40 offset1:60
	v_cmp_gt_u32_e64 s[6:7], 16, v104
	v_mov_b32_e32 v37, 1.0
	v_mov_b32_e32 v20, 0
	v_mov_b32_e32 v19, 0
	v_mov_b32_e32 v18, 0
	v_mov_b32_e32 v36, 0
